# speedup vs baseline: 1.0068x; 1.0014x over previous
_Z11prep_kernelPKfS0_S0_S0_Pc:
	s_load_dwordx2 s[4:5], s[0:1], 0x20
	s_load_dwordx2 s[24:25], s[0:1], 0x8
	v_lshl_or_b32 v2, s2, 8, v0
	s_mov_b32 s2, 0x371ff
	v_cmp_lt_i32_e32 vcc, s2, v2
	s_and_saveexec_b64 s[2:3], vcc
	s_xor_b64 s[6:7], exec, s[2:3]
	s_cbranch_execnz .LBB0_3
	s_andn2_saveexec_b64 s[2:3], s[6:7]
	s_cbranch_execnz .LBB0_60

.LBB0_60:
	v_ashrrev_i32_e32 v1, 6, v2
	s_mov_b32 s2, 0x55555556
	v_mul_hi_i32 v3, v1, s2
	v_lshrrev_b32_e32 v4, 31, v3
	v_add_u32_e32 v3, v3, v4
	s_mov_b32 s2, 0x5397829d
	v_mul_hi_i32 v5, v3, s2
	v_lshrrev_b32_e32 v6, 31, v5
	v_lshrrev_b32_e32 v5, 4, v5
	v_lshl_add_u32 v4, v3, 1, v3
	v_add_u32_e32 v5, v5, v6
	s_mov_b32 s2, 0x6f74ae27
	s_waitcnt lgkmcnt(0)
	s_mov_b64 s[0:1], s[24:25]
	v_sub_u32_e32 v4, v1, v4
	v_mul_lo_u32 v5, v5, 49
	v_mul_hi_i32 v1, v1, s2
	v_sub_u32_e32 v3, v3, v5
	v_lshrrev_b32_e32 v5, 31, v1
	v_lshrrev_b32_e32 v1, 6, v1
	v_add_u32_e32 v1, v1, v5
	v_and_b32_e32 v5, 31, v0
	v_lshl_or_b32 v6, v4, 5, v5
	v_lshrrev_b32_e32 v0, 2, v0
	v_mul_i32_i24_e32 v1, 0x310, v1
	s_movk_i32 s2, 0x55
	v_and_or_b32 v0, v0, 8, v1
	v_ashrrev_i32_e32 v7, 31, v6
	v_cmp_gt_i32_e32 vcc, s2, v6
	v_lshl_add_u32 v5, v3, 4, v0
	s_waitcnt lgkmcnt(0)
	v_lshl_add_u64 v[0:1], v[6:7], 2, s[0:1]
	v_mov_b32_e32 v3, 0
	v_mov_b32_e32 v4, 0
	v_mov_b32_e32 v7, 0
	v_mov_b32_e32 v6, 0
	v_mov_b32_e32 v9, 0
	v_mov_b32_e32 v8, 0
	v_mov_b32_e32 v11, 0
	v_mov_b32_e32 v10, 0
	s_and_saveexec_b64 s[0:1], vcc
	s_movk_i32 s2, 0x154
	v_mad_i64_i32 v[12:13], s[2:3], v5, s2, v[0:1]
	global_load_dword v3, v[12:13], off
	global_load_dword v4, v[12:13], off offset:340
	global_load_dword v7, v[12:13], off offset:680
	global_load_dword v6, v[12:13], off offset:1020
	global_load_dword v9, v[12:13], off offset:1360
	global_load_dword v8, v[12:13], off offset:1700
	global_load_dword v11, v[12:13], off offset:2040
	global_load_dword v10, v[12:13], off offset:2380
	s_waitcnt vmcnt(0)
	v_cvt_f16_f32_e32 v3, v3
	v_cvt_f16_f32_e32 v4, v4
	v_cvt_f16_f32_e32 v7, v7
	v_cvt_f16_f32_e32 v6, v6
	v_cvt_f16_f32_e32 v9, v9
	v_cvt_f16_f32_e32 v8, v8
	v_cvt_f16_f32_e32 v11, v11
	v_cvt_f16_f32_e32 v10, v10

	.amdhsa_kernel _Z11prep_kernelPKfS0_S0_S0_Pc
		.amdhsa_group_segment_fixed_size 0
		.amdhsa_private_segment_fixed_size 0
		.amdhsa_kernarg_size 40
		.amdhsa_user_sgpr_count 2
		.amdhsa_user_sgpr_dispatch_ptr 0
		.amdhsa_user_sgpr_queue_ptr 0
		.amdhsa_user_sgpr_kernarg_segment_ptr 1
		.amdhsa_user_sgpr_dispatch_id 0
		.amdhsa_user_sgpr_kernarg_preload_length 0
		.amdhsa_user_sgpr_kernarg_preload_offset 0
		.amdhsa_user_sgpr_private_segment_size 0
		.amdhsa_uses_dynamic_stack 0
		.amdhsa_enable_private_segment 0
		.amdhsa_system_sgpr_workgroup_id_x 1
		.amdhsa_system_sgpr_workgroup_id_y 0
		.amdhsa_system_sgpr_workgroup_id_z 0
		.amdhsa_system_sgpr_workgroup_info 0
		.amdhsa_system_vgpr_workitem_id 0
		.amdhsa_next_free_vgpr 20
		.amdhsa_next_free_sgpr 26
		.amdhsa_accum_offset 20
		.amdhsa_reserve_vcc 1
		.amdhsa_float_round_mode_32 0
		.amdhsa_float_round_mode_16_64 0
		.amdhsa_float_denorm_mode_32 3
		.amdhsa_float_denorm_mode_16_64 3
		.amdhsa_dx10_clamp 1
		.amdhsa_ieee_mode 1
		.amdhsa_fp16_overflow 0
		.amdhsa_tg_split 0
		.amdhsa_exception_fp_ieee_invalid_op 0
		.amdhsa_exception_fp_denorm_src 0
		.amdhsa_exception_fp_ieee_div_zero 0
		.amdhsa_exception_fp_ieee_overflow 0
		.amdhsa_exception_fp_ieee_underflow 0
		.amdhsa_exception_fp_ieee_inexact 0
		.amdhsa_exception_int_div_zero 0
	.end_amdhsa_kernel
